# c46: c41 + OUT0/D0/OUT1 GEMM prologues: the wait before the residual conversion only covers the residual loads (second K-tile's LDS-DMA loads stay in flight, as in the fp8 phases)
# speedup vs baseline: 1.0040x; 1.0040x over previous
; #define PG8_STAGE(bufoff, gbase, voff) do { _Pragma("unroll") for (int _i = 0; _i < 2; ++_i) \
;         __builtin_amdgcn_global_load_lds((const unsigned*)((const char*)(gbase) + (voff)[_i]), (PG8_LAS unsigned*)(lds + (bufoff) + ldsw + _i * 8192), 16, 0, 0); } while (0)
; #define PG8_WAIT_V(n) asm volatile("s_waitcnt vmcnt(" #n ")" ::: "memory")
; #define PG8_BAR __builtin_amdgcn_s_barrier()
; template <class Epi, class Sched, bool ALIGN_EPI = false, bool SP2 = false, bool F8 = false>
; __device__ __forceinline__ void gemm_phase(PG8_LAS unsigned char* lds, const Gemm g, const Sched& S, const Epi& E) {
;     ...
;     for (int i = 0; i < 2; ++i) { int R, C; stage_rc(tid * 16 + i * 8192, R, C); const int Rb = Epi::PERM ? ((R & ~31) + perm32(R & 31)) : R;
;         voffA[i] = (unsigned)(R * K + C) * 2u; voffB[i] = (unsigned)(Rb * K + C) * 2u; }
;     const size_t kstep = (size_t)(BK * 2);
;     const size_t hstep = (size_t)HALF * K * 2;
;     const size_t tstep = 2 * hstep;
;     const unsigned ldsw = (unsigned)wid * 1024u;
;     const int aoff = lds_byte(wr * 64 + fr, fq * 8), boff = lds_byte(wc * 32 + fr, fq * 8);
;     ...
;         PG8_STAGE(PG8_SB(0, 0), cB, voffB); PG8_STAGE(PG8_SB(0, 1), cB + hstep, voffB); PG8_STAGE(PG8_SA(0, 0), cA, voffA); PG8_STAGE(PG8_SA(0, 1), cA + hstep, voffA);
;         if (wr == 1) PG8_BAR;
;         PG8_WAIT_V(2); PG8_BAR;
;         PG8_STAGE(PG8_SB(1, 0), cB + kstep, voffB); PG8_STAGE(PG8_SA(1, 0), cA + kstep, voffA); PG8_STAGE(PG8_SB(1, 1), cB + hstep + kstep, voffB);
;         PG8_WAIT_V(6); PG8_BAR;
.LBB0_428:
	s_add_u32 s38, s34, 0xec00000
	s_mov_b64 s[40:41], 0x80
	s_addc_u32 s39, s35, 0
	s_add_i32 m0, s19, 0x18000
	v_lshl_add_u64 v[138:139], v[138:139], 0, s[40:41]
	s_lshl_b32 s0, s6, 13
	s_lshl_b32 s1, s4, 12
	s_waitcnt vmcnt(2)
	s_barrier
	global_load_lds_dwordx4 v[138:139], off
	v_lshl_add_u64 v[128:129], v[128:129], 0, s[40:41]
	s_add_i32 m0, s19, 0x1a000
	s_add_i32 s87, s19, 0x8000
	s_add_i32 s88, s19, 0xa000
	global_load_lds_dwordx4 v[128:129], off
	v_lshl_add_u64 v[116:117], v[116:117], 0, s[40:41]
	s_mov_b32 m0, s87
	s_add_u32 s6, s70, 0x40080
	global_load_lds_dwordx4 v[116:117], off
	v_lshl_add_u64 v[116:117], v[126:127], 0, s[40:41]
	s_mov_b32 m0, s88
	s_addc_u32 s7, s71, 0
	global_load_lds_dwordx4 v[116:117], off
	s_add_i32 m0, s19, 0x1c000
	v_lshl_add_u64 v[116:117], s[6:7], 0, v[132:133]
	global_load_lds_dwordx4 v[116:117], off
	v_lshl_add_u64 v[116:117], s[6:7], 0, v[136:137]
	s_add_i32 m0, s19, 0x1e000
	v_lshlrev_b32_e32 v138, 6, v150
	global_load_lds_dwordx4 v[116:117], off
	v_lshlrev_b32_e32 v139, 4, v142
	s_movk_i32 s6, 0x3c0
	v_lshlrev_b32_e32 v149, 2, v150
	v_and_or_b32 v138, v138, s6, v139
	v_and_b32_e32 v149, 32, v149
	v_bitop3_b32 v149, v138, s0, v149 bitop3:0xde
	v_lshl_or_b32 v138, v148, 6, v139
	v_lshlrev_b32_e32 v139, 2, v148
	v_and_b32_e32 v139, 32, v139
	v_bitop3_b32 v158, v138, s1, v139 bitop3:0xde
	v_lshlrev_b32_e32 v138, 14, v140
	v_and_b32_e32 v139, 1, v140
	v_lshlrev_b32_e32 v140, 14, v144
	v_and_b32_e32 v138, 0xffff8000, v138
	v_and_b32_e32 v140, 0xffff8000, v140
	s_movk_i32 s0, 0x100
	s_cmpk_lt_u32 s3, 0x100
	v_lshl_add_u32 v138, v141, 11, v138
	v_lshl_add_u32 v140, v145, 11, v140
	v_and_b32_e32 v141, 1, v144
	s_waitcnt vmcnt(6)
	s_cselect_b64 s[42:43], -1, 0
	v_cmp_gt_u32_e64 s[10:11], s0, v0
	s_lshl_b32 s0, s4, 2
	v_lshl_or_b32 v138, v139, 6, v138
	v_lshl_or_b32 v140, v141, 6, v140
	s_mov_b64 s[6:7], 0x40080
	v_lshlrev_b32_e32 v148, 4, v150
	v_lshlrev_b32_e32 v166, 4, v151
	v_lshlrev_b32_e32 v167, 4, v152
	v_lshlrev_b32_e32 v168, 4, v153
	v_lshlrev_b32_e32 v169, 4, v154
	v_lshlrev_b32_e32 v170, 4, v155
	v_lshlrev_b32_e32 v171, 4, v156
	v_lshlrev_b32_e32 v172, 4, v157
	v_lshlrev_b32_e32 v173, 4, v0
	s_or_b32 s0, s0, 0x20540
	v_lshl_add_u32 v138, v143, 1, v138
	v_mov_b32_e32 v139, v133
	v_lshl_add_u32 v140, v146, 1, v140
	v_mov_b32_e32 v141, v133
	v_mbcnt_lo_u32_b32 v146, -1, 0
	s_waitcnt vmcnt(6)
;     __device__ __forceinline__ void init(f32x4 (&acc)[2][2][4][2], const Unit& u, int wr, int wc, int fr, int fq) const {
;     ...
;                     } else { const u32x4 w = *(const u32x4*)(bbase + off + bj * HALF);
;                         acc[ai][bj][m][0] = (f32x4){__builtin_bit_cast(float, w.x << 16), __builtin_bit_cast(float, w.x & 0xffff0000u), __builtin_bit_cast(float, w.y << 16), __builtin_bit_cast(float, w.y & 0xffff0000u)};
;                         acc[ai][bj][m][1] = (f32x4){__builtin_bit_cast(float, w.z << 16), __builtin_bit_cast(float, w.z & 0xffff0000u), __builtin_bit_cast(float, w.w << 16), __builtin_bit_cast(float, w.w & 0xffff0000u)}; } } }
	v_lshlrev_b32_e32 v22, 16, v2
	v_and_b32_e32 v23, 0xffff0000, v2
	v_lshlrev_b32_e32 v24, 16, v3
	v_and_b32_e32 v25, 0xffff0000, v3
	v_lshlrev_b32_e32 v30, 16, v4
	v_and_b32_e32 v31, 0xffff0000, v4
	v_lshlrev_b32_e32 v32, 16, v5
	v_and_b32_e32 v33, 0xffff0000, v5
	v_lshlrev_b32_e32 v2, 16, v6
	v_and_b32_e32 v3, 0xffff0000, v6
	v_lshlrev_b32_e32 v4, 16, v7
	v_and_b32_e32 v5, 0xffff0000, v7
	v_lshlrev_b32_e32 v6, 16, v8
	v_and_b32_e32 v7, 0xffff0000, v8
	v_lshlrev_b32_e32 v8, 16, v9
	v_and_b32_e32 v9, 0xffff0000, v9
	v_lshlrev_b32_e32 v46, 16, v10
	v_and_b32_e32 v47, 0xffff0000, v10
	v_lshlrev_b32_e32 v48, 16, v11
	v_and_b32_e32 v49, 0xffff0000, v11
	v_lshlrev_b32_e32 v54, 16, v12
	v_and_b32_e32 v55, 0xffff0000, v12
	v_lshlrev_b32_e32 v56, 16, v13
	v_and_b32_e32 v57, 0xffff0000, v13
	v_lshlrev_b32_e32 v10, 16, v14
	v_and_b32_e32 v11, 0xffff0000, v14
	v_lshlrev_b32_e32 v12, 16, v15
	v_and_b32_e32 v13, 0xffff0000, v15
	v_lshlrev_b32_e32 v14, 16, v16
	v_and_b32_e32 v15, 0xffff0000, v16
	v_lshlrev_b32_e32 v16, 16, v17
	v_and_b32_e32 v17, 0xffff0000, v17
	v_lshlrev_b32_e32 v78, 16, v34
	v_and_b32_e32 v79, 0xffff0000, v34
	v_lshlrev_b32_e32 v80, 16, v35
	v_and_b32_e32 v81, 0xffff0000, v35
	v_lshlrev_b32_e32 v86, 16, v36
	v_and_b32_e32 v87, 0xffff0000, v36
	v_lshlrev_b32_e32 v88, 16, v37
	v_and_b32_e32 v89, 0xffff0000, v37
	v_lshlrev_b32_e32 v34, 16, v38
	v_and_b32_e32 v35, 0xffff0000, v38
	v_lshlrev_b32_e32 v36, 16, v39
	v_and_b32_e32 v37, 0xffff0000, v39
	v_lshlrev_b32_e32 v38, 16, v40
	v_and_b32_e32 v39, 0xffff0000, v40
	v_lshlrev_b32_e32 v40, 16, v41
	v_and_b32_e32 v41, 0xffff0000, v41
	v_lshlrev_b32_e32 v98, 16, v58
	v_and_b32_e32 v99, 0xffff0000, v58
	v_lshlrev_b32_e32 v100, 16, v59
	v_and_b32_e32 v101, 0xffff0000, v59
	v_lshlrev_b32_e32 v102, 16, v60
	v_and_b32_e32 v103, 0xffff0000, v60
	v_lshlrev_b32_e32 v104, 16, v61
	v_and_b32_e32 v105, 0xffff0000, v61
	v_lshlrev_b32_e32 v58, 16, v18
	v_and_b32_e32 v59, 0xffff0000, v18
	v_lshlrev_b32_e32 v60, 16, v19
	v_and_b32_e32 v61, 0xffff0000, v19
	v_lshlrev_b32_e32 v62, 16, v20
	v_and_b32_e32 v63, 0xffff0000, v20
	v_lshlrev_b32_e32 v64, 16, v21
	v_and_b32_e32 v65, 0xffff0000, v21
	v_lshlrev_b32_e32 v66, 16, v70
	v_and_b32_e32 v67, 0xffff0000, v70
	v_lshlrev_b32_e32 v68, 16, v71
	v_and_b32_e32 v69, 0xffff0000, v71
	v_lshlrev_b32_e32 v70, 16, v72
	v_and_b32_e32 v71, 0xffff0000, v72
	v_lshlrev_b32_e32 v72, 16, v73
	v_and_b32_e32 v73, 0xffff0000, v73
	v_lshlrev_b32_e32 v18, 16, v26
	v_and_b32_e32 v19, 0xffff0000, v26
	v_lshlrev_b32_e32 v20, 16, v27
	v_and_b32_e32 v21, 0xffff0000, v27
	v_lshlrev_b32_e32 v26, 16, v28
	v_and_b32_e32 v27, 0xffff0000, v28
	v_lshlrev_b32_e32 v28, 16, v29
	v_and_b32_e32 v29, 0xffff0000, v29
	v_lshlrev_b32_e32 v90, 16, v42
	v_and_b32_e32 v91, 0xffff0000, v42
	v_lshlrev_b32_e32 v92, 16, v43
	v_and_b32_e32 v93, 0xffff0000, v43
	v_lshlrev_b32_e32 v94, 16, v44
	v_and_b32_e32 v95, 0xffff0000, v44
	v_lshlrev_b32_e32 v96, 16, v45
	v_and_b32_e32 v97, 0xffff0000, v45
	v_lshlrev_b32_e32 v42, 16, v50
	v_and_b32_e32 v43, 0xffff0000, v50
	v_lshlrev_b32_e32 v44, 16, v51
	v_and_b32_e32 v45, 0xffff0000, v51
	v_lshlrev_b32_e32 v50, 16, v52
	v_and_b32_e32 v51, 0xffff0000, v52
	v_lshlrev_b32_e32 v52, 16, v53
	v_and_b32_e32 v53, 0xffff0000, v53
	v_lshlrev_b32_e32 v106, 16, v74
	v_and_b32_e32 v107, 0xffff0000, v74
	v_lshlrev_b32_e32 v108, 16, v75
	v_and_b32_e32 v109, 0xffff0000, v75
	v_lshlrev_b32_e32 v110, 16, v76
	v_and_b32_e32 v111, 0xffff0000, v76
	v_lshlrev_b32_e32 v112, 16, v77
	v_and_b32_e32 v113, 0xffff0000, v77
	v_lshlrev_b32_e32 v74, 16, v82
	v_and_b32_e32 v75, 0xffff0000, v82
	v_lshlrev_b32_e32 v76, 16, v83
	v_and_b32_e32 v77, 0xffff0000, v83
	v_lshlrev_b32_e32 v82, 16, v84
	v_and_b32_e32 v83, 0xffff0000, v84
	v_lshlrev_b32_e32 v84, 16, v85
	v_and_b32_e32 v85, 0xffff0000, v85
	v_lshlrev_b32_e32 v114, 16, v122
	v_and_b32_e32 v115, 0xffff0000, v122
	v_lshlrev_b32_e32 v116, 16, v123
	v_and_b32_e32 v117, 0xffff0000, v123
	v_lshlrev_b32_e32 v126, 16, v124
	v_and_b32_e32 v127, 0xffff0000, v124
	v_lshlrev_b32_e32 v128, 16, v125
	v_and_b32_e32 v129, 0xffff0000, v125
	v_lshlrev_b32_e32 v122, 16, v118
	v_and_b32_e32 v123, 0xffff0000, v118
	v_lshlrev_b32_e32 v124, 16, v119
	v_and_b32_e32 v125, 0xffff0000, v119
	v_lshlrev_b32_e32 v118, 16, v120
	v_and_b32_e32 v119, 0xffff0000, v120
	v_lshlrev_b32_e32 v120, 16, v121
	v_and_b32_e32 v121, 0xffff0000, v121
	v_cmp_eq_u32_e64 s[8:9], 0, v142
	s_ashr_i32 s89, s2, 31
	v_or_b32_e32 v159, s5, v147
	v_lshl_add_u64 v[138:139], v[138:139], 0, s[6:7]
	v_lshl_add_u64 v[140:141], v[140:141], 0, s[6:7]
	v_mov_b64_e32 v[142:143], 0x100
	v_mov_b64_e32 v[144:145], 0xff
	s_add_i32 s90, 0, 0x10000
	s_add_i32 s91, 0, 0x14000
	v_add_u32_e32 v160, 0, v149
	v_mbcnt_hi_u32_b32 v161, -1, v146
	v_add_u32_e32 v165, s0, v148
	v_add_u32_e32 v166, s0, v166
	v_add_u32_e32 v167, s0, v167
	v_add_u32_e32 v168, s0, v168
	v_add_u32_e32 v169, s0, v169
	v_add_u32_e32 v170, s0, v170
	v_add_u32_e32 v171, s0, v171
	v_add_u32_e32 v172, s0, v172
	v_add_u32_e32 v173, 0x20540, v173
	s_barrier
	s_branch .LBB0_430

; #define PG8_STAGE(bufoff, gbase, voff) do { _Pragma("unroll") for (int _i = 0; _i < 2; ++_i) \
;         __builtin_amdgcn_global_load_lds((const unsigned*)((const char*)(gbase) + (voff)[_i]), (PG8_LAS unsigned*)(lds + (bufoff) + ldsw + _i * 8192), 16, 0, 0); } while (0)
; #define PG8_WAIT_V(n) asm volatile("s_waitcnt vmcnt(" #n ")" ::: "memory")
; #define PG8_BAR __builtin_amdgcn_s_barrier()
; template <class Epi, class Sched, bool ALIGN_EPI = false, bool SP2 = false, bool F8 = false>
; __device__ __forceinline__ void gemm_phase(PG8_LAS unsigned char* lds, const Gemm g, const Sched& S, const Epi& E) {
;     ...
;     for (int i = 0; i < 2; ++i) { int R, C; stage_rc(tid * 16 + i * 8192, R, C); const int Rb = Epi::PERM ? ((R & ~31) + perm32(R & 31)) : R;
;         voffA[i] = (unsigned)(R * K + C) * 2u; voffB[i] = (unsigned)(Rb * K + C) * 2u; }
;     const size_t kstep = (size_t)(BK * 2);
;     const size_t hstep = (size_t)HALF * K * 2;
;     const size_t tstep = 2 * hstep;
;     const unsigned ldsw = (unsigned)wid * 1024u;
;     const int aoff = lds_byte(wr * 64 + fr, fq * 8), boff = lds_byte(wc * 32 + fr, fq * 8);
;     ...
;         PG8_STAGE(PG8_SB(0, 0), cB, voffB); PG8_STAGE(PG8_SB(0, 1), cB + hstep, voffB); PG8_STAGE(PG8_SA(0, 0), cA, voffA); PG8_STAGE(PG8_SA(0, 1), cA + hstep, voffA);
;         if (wr == 1) PG8_BAR;
;         PG8_WAIT_V(2); PG8_BAR;
;         PG8_STAGE(PG8_SB(1, 0), cB + kstep, voffB); PG8_STAGE(PG8_SA(1, 0), cA + kstep, voffA); PG8_STAGE(PG8_SB(1, 1), cB + hstep + kstep, voffB);
;         PG8_WAIT_V(6); PG8_BAR;
.LBB0_661:
	s_lshl_b32 s0, s7, 13
	s_lshl_b32 s1, s4, 12
	s_add_u32 s38, s34, 0xed00000
	s_addc_u32 s39, s35, 0
	s_add_u32 s40, s34, 0x1c000000
	s_mov_b64 s[42:43], 0x80
	s_addc_u32 s41, s35, 0
	s_add_i32 m0, s83, 0x18000
	v_lshl_add_u64 v[140:141], v[140:141], 0, s[42:43]
	s_waitcnt vmcnt(2)
	s_barrier
	global_load_lds_dwordx4 v[140:141], off
	v_lshl_add_u64 v[138:139], v[138:139], 0, s[42:43]
	s_add_i32 m0, s83, 0x1a000
	s_add_i32 s87, s83, 0x8000
	s_add_i32 s88, s83, 0xa000
	global_load_lds_dwordx4 v[138:139], off
	v_lshl_add_u64 v[126:127], v[126:127], 0, s[42:43]
	s_mov_b32 m0, s87
	s_add_u32 s8, s50, 0xe0080
	global_load_lds_dwordx4 v[126:127], off
	v_lshl_add_u64 v[126:127], v[128:129], 0, s[42:43]
	s_mov_b32 m0, s88
	s_addc_u32 s9, s51, 0
	global_load_lds_dwordx4 v[126:127], off
	s_add_i32 m0, s83, 0x1c000
	v_lshl_add_u64 v[126:127], s[8:9], 0, v[132:133]
	global_load_lds_dwordx4 v[126:127], off
	v_lshl_add_u64 v[126:127], s[8:9], 0, v[136:137]
	s_add_i32 m0, s83, 0x1e000
	v_lshlrev_b32_e32 v138, 6, v150
	global_load_lds_dwordx4 v[126:127], off
	v_lshlrev_b32_e32 v139, 4, v144
	s_movk_i32 s7, 0x3c0
	v_lshlrev_b32_e32 v140, 2, v150
	v_and_or_b32 v138, v138, s7, v139
	v_and_b32_e32 v140, 32, v140
	v_bitop3_b32 v161, v138, s0, v140 bitop3:0xde
	v_lshl_or_b32 v138, v158, 6, v139
	v_lshlrev_b32_e32 v139, 2, v158
	v_and_b32_e32 v139, 32, v139
	v_bitop3_b32 v158, v138, s1, v139 bitop3:0xde
	s_movk_i32 s0, 0x100
	s_cmpk_lt_u32 s3, 0x100
	v_lshrrev_b32_e32 v139, 1, v142
	v_mul_lo_u32 v138, v145, s5
	s_mov_b32 s1, 0xe000
	v_lshrrev_b32_e32 v141, 1, v147
	v_mul_lo_u32 v140, v148, s5
	s_cselect_b64 s[44:45], -1, 0
	v_cmp_gt_u32_e64 s[10:11], s0, v0
	s_lshl_b32 s0, s4, 2
	v_or_b32_e32 v159, s6, v159
	v_mad_u64_u32 v[138:139], s[6:7], v139, s1, v[138:139]
	v_mad_u64_u32 v[140:141], s[4:5], v141, s1, v[140:141]
	s_waitcnt vmcnt(6)
	v_or_b32_e32 v138, v138, v143
	v_or_b32_e32 v140, v140, v149
	s_mov_b64 s[12:13], 0xe0080
	v_lshlrev_b32_e32 v165, 4, v150
	v_lshlrev_b32_e32 v166, 4, v151
	v_lshlrev_b32_e32 v167, 4, v152
	v_lshlrev_b32_e32 v168, 4, v153
	v_lshlrev_b32_e32 v169, 4, v154
	v_lshlrev_b32_e32 v170, 4, v155
	v_lshlrev_b32_e32 v171, 4, v156
	v_lshlrev_b32_e32 v172, 4, v157
	v_lshlrev_b32_e32 v173, 4, v0
	s_or_b32 s0, s0, 0x20540
	v_add_lshl_u32 v138, v138, v146, 1
	v_mov_b32_e32 v139, v133
	v_add_lshl_u32 v140, v140, v160, 1
	v_mov_b32_e32 v141, v133
	v_mbcnt_lo_u32_b32 v146, -1, 0
	s_waitcnt vmcnt(6)
;     __device__ __forceinline__ void init(f32x4 (&acc)[2][2][4][2], const Unit& u, int wr, int wc, int fr, int fq) const {
;     ...
;                     } else { const u32x4 w = *(const u32x4*)(bbase + off + bj * HALF);
;                         acc[ai][bj][m][0] = (f32x4){__builtin_bit_cast(float, w.x << 16), __builtin_bit_cast(float, w.x & 0xffff0000u), __builtin_bit_cast(float, w.y << 16), __builtin_bit_cast(float, w.y & 0xffff0000u)};
;                         acc[ai][bj][m][1] = (f32x4){__builtin_bit_cast(float, w.z << 16), __builtin_bit_cast(float, w.z & 0xffff0000u), __builtin_bit_cast(float, w.w << 16), __builtin_bit_cast(float, w.w & 0xffff0000u)}; } } }
	v_lshlrev_b32_e32 v22, 16, v2
	v_and_b32_e32 v23, 0xffff0000, v2
	v_lshlrev_b32_e32 v24, 16, v3
	v_and_b32_e32 v25, 0xffff0000, v3
	v_lshlrev_b32_e32 v30, 16, v4
	v_and_b32_e32 v31, 0xffff0000, v4
	v_lshlrev_b32_e32 v32, 16, v5
	v_and_b32_e32 v33, 0xffff0000, v5
	v_lshlrev_b32_e32 v2, 16, v6
	v_and_b32_e32 v3, 0xffff0000, v6
	v_lshlrev_b32_e32 v4, 16, v7
	v_and_b32_e32 v5, 0xffff0000, v7
	v_lshlrev_b32_e32 v6, 16, v8
	v_and_b32_e32 v7, 0xffff0000, v8
	v_lshlrev_b32_e32 v8, 16, v9
	v_and_b32_e32 v9, 0xffff0000, v9
	v_lshlrev_b32_e32 v46, 16, v10
	v_and_b32_e32 v47, 0xffff0000, v10
	v_lshlrev_b32_e32 v48, 16, v11
	v_and_b32_e32 v49, 0xffff0000, v11
	v_lshlrev_b32_e32 v54, 16, v12
	v_and_b32_e32 v55, 0xffff0000, v12
	v_lshlrev_b32_e32 v56, 16, v13
	v_and_b32_e32 v57, 0xffff0000, v13
	v_lshlrev_b32_e32 v10, 16, v14
	v_and_b32_e32 v11, 0xffff0000, v14
	v_lshlrev_b32_e32 v12, 16, v15
	v_and_b32_e32 v13, 0xffff0000, v15
	v_lshlrev_b32_e32 v14, 16, v16
	v_and_b32_e32 v15, 0xffff0000, v16
	v_lshlrev_b32_e32 v16, 16, v17
	v_and_b32_e32 v17, 0xffff0000, v17
	v_lshlrev_b32_e32 v78, 16, v34
	v_and_b32_e32 v79, 0xffff0000, v34
	v_lshlrev_b32_e32 v80, 16, v35
	v_and_b32_e32 v81, 0xffff0000, v35
	v_lshlrev_b32_e32 v86, 16, v36
	v_and_b32_e32 v87, 0xffff0000, v36
	v_lshlrev_b32_e32 v88, 16, v37
	v_and_b32_e32 v89, 0xffff0000, v37
	v_lshlrev_b32_e32 v34, 16, v38
	v_and_b32_e32 v35, 0xffff0000, v38
	v_lshlrev_b32_e32 v36, 16, v39
	v_and_b32_e32 v37, 0xffff0000, v39
	v_lshlrev_b32_e32 v38, 16, v40
	v_and_b32_e32 v39, 0xffff0000, v40
	v_lshlrev_b32_e32 v40, 16, v41
	v_and_b32_e32 v41, 0xffff0000, v41
	v_lshlrev_b32_e32 v98, 16, v58
	v_and_b32_e32 v99, 0xffff0000, v58
	v_lshlrev_b32_e32 v100, 16, v59
	v_and_b32_e32 v101, 0xffff0000, v59
	v_lshlrev_b32_e32 v102, 16, v60
	v_and_b32_e32 v103, 0xffff0000, v60
	v_lshlrev_b32_e32 v104, 16, v61
	v_and_b32_e32 v105, 0xffff0000, v61
	v_lshlrev_b32_e32 v58, 16, v18
	v_and_b32_e32 v59, 0xffff0000, v18
	v_lshlrev_b32_e32 v60, 16, v19
	v_and_b32_e32 v61, 0xffff0000, v19
	v_lshlrev_b32_e32 v62, 16, v20
	v_and_b32_e32 v63, 0xffff0000, v20
	v_lshlrev_b32_e32 v64, 16, v21
	v_and_b32_e32 v65, 0xffff0000, v21
	v_lshlrev_b32_e32 v66, 16, v70
	v_and_b32_e32 v67, 0xffff0000, v70
	v_lshlrev_b32_e32 v68, 16, v71
	v_and_b32_e32 v69, 0xffff0000, v71
	v_lshlrev_b32_e32 v70, 16, v72
	v_and_b32_e32 v71, 0xffff0000, v72
	v_lshlrev_b32_e32 v72, 16, v73
	v_and_b32_e32 v73, 0xffff0000, v73
	v_lshlrev_b32_e32 v18, 16, v26
	v_and_b32_e32 v19, 0xffff0000, v26
	v_lshlrev_b32_e32 v20, 16, v27
	v_and_b32_e32 v21, 0xffff0000, v27
	v_lshlrev_b32_e32 v26, 16, v28
	v_and_b32_e32 v27, 0xffff0000, v28
	v_lshlrev_b32_e32 v28, 16, v29
	v_and_b32_e32 v29, 0xffff0000, v29
	v_lshlrev_b32_e32 v90, 16, v42
	v_and_b32_e32 v91, 0xffff0000, v42
	v_lshlrev_b32_e32 v92, 16, v43
	v_and_b32_e32 v93, 0xffff0000, v43
	v_lshlrev_b32_e32 v94, 16, v44
	v_and_b32_e32 v95, 0xffff0000, v44
	v_lshlrev_b32_e32 v96, 16, v45
	v_and_b32_e32 v97, 0xffff0000, v45
	v_lshlrev_b32_e32 v42, 16, v50
	v_and_b32_e32 v43, 0xffff0000, v50
	v_lshlrev_b32_e32 v44, 16, v51
	v_and_b32_e32 v45, 0xffff0000, v51
	v_lshlrev_b32_e32 v50, 16, v52
	v_and_b32_e32 v51, 0xffff0000, v52
	v_lshlrev_b32_e32 v52, 16, v53
	v_and_b32_e32 v53, 0xffff0000, v53
	v_lshlrev_b32_e32 v106, 16, v74
	v_and_b32_e32 v107, 0xffff0000, v74
	v_lshlrev_b32_e32 v108, 16, v75
	v_and_b32_e32 v109, 0xffff0000, v75
	v_lshlrev_b32_e32 v110, 16, v76
	v_and_b32_e32 v111, 0xffff0000, v76
	v_lshlrev_b32_e32 v112, 16, v77
	v_and_b32_e32 v113, 0xffff0000, v77
	v_lshlrev_b32_e32 v74, 16, v82
	v_and_b32_e32 v75, 0xffff0000, v82
	v_lshlrev_b32_e32 v76, 16, v83
	v_and_b32_e32 v77, 0xffff0000, v83
	v_lshlrev_b32_e32 v82, 16, v84
	v_and_b32_e32 v83, 0xffff0000, v84
	v_lshlrev_b32_e32 v84, 16, v85
	v_and_b32_e32 v85, 0xffff0000, v85
	v_lshlrev_b32_e32 v114, 16, v122
	v_and_b32_e32 v115, 0xffff0000, v122
	v_lshlrev_b32_e32 v116, 16, v123
	v_and_b32_e32 v117, 0xffff0000, v123
	v_lshlrev_b32_e32 v126, 16, v124
	v_and_b32_e32 v127, 0xffff0000, v124
	v_lshlrev_b32_e32 v128, 16, v125
	v_and_b32_e32 v129, 0xffff0000, v125
	v_lshlrev_b32_e32 v122, 16, v118
	v_and_b32_e32 v123, 0xffff0000, v118
	v_lshlrev_b32_e32 v124, 16, v119
	v_and_b32_e32 v125, 0xffff0000, v119
	v_lshlrev_b32_e32 v118, 16, v120
	v_and_b32_e32 v119, 0xffff0000, v120
	v_lshlrev_b32_e32 v120, 16, v121
	v_and_b32_e32 v121, 0xffff0000, v121
	v_cmp_eq_u32_e64 s[8:9], 0, v144
	s_ashr_i32 s89, s2, 31
	v_lshl_add_u64 v[138:139], v[138:139], 0, s[12:13]
	v_lshl_add_u64 v[140:141], v[140:141], 0, s[12:13]
	v_mov_b64_e32 v[142:143], 0x100
	v_mov_b64_e32 v[144:145], 0xff
	s_add_i32 s90, 0, 0x10000
	s_add_i32 s91, 0, 0x14000
	v_add_u32_e32 v160, 0, v161
	v_add_u32_e32 v161, s0, v165
	v_add_u32_e32 v165, s0, v166
	v_add_u32_e32 v166, s0, v167
	v_add_u32_e32 v167, s0, v168
	v_add_u32_e32 v168, s0, v169
	v_add_u32_e32 v169, s0, v170
	v_add_u32_e32 v170, s0, v171
	v_add_u32_e32 v171, s0, v172
	v_add_u32_e32 v172, 0x20540, v173
	v_mbcnt_hi_u32_b32 v173, -1, v146
	s_barrier
	s_branch .LBB0_663

; #define PG8_STAGE(bufoff, gbase, voff) do { _Pragma("unroll") for (int _i = 0; _i < 2; ++_i) \
;         __builtin_amdgcn_global_load_lds((const unsigned*)((const char*)(gbase) + (voff)[_i]), (PG8_LAS unsigned*)(lds + (bufoff) + ldsw + _i * 8192), 16, 0, 0); } while (0)
; #define PG8_WAIT_V(n) asm volatile("s_waitcnt vmcnt(" #n ")" ::: "memory")
; #define PG8_BAR __builtin_amdgcn_s_barrier()
;     __device__ __forceinline__ void init(f32x4 (&acc)[2][2][4][2], const Unit& u, int wr, int wc, int fr, int fq) const {
;     ...
;                     } else { const u32x4 w = *(const u32x4*)(bbase + off + bj * HALF);
;                         acc[ai][bj][m][0] = (f32x4){__builtin_bit_cast(float, w.x << 16), __builtin_bit_cast(float, w.x & 0xffff0000u), __builtin_bit_cast(float, w.y << 16), __builtin_bit_cast(float, w.y & 0xffff0000u)};
;                         acc[ai][bj][m][1] = (f32x4){__builtin_bit_cast(float, w.z << 16), __builtin_bit_cast(float, w.z & 0xffff0000u), __builtin_bit_cast(float, w.w << 16), __builtin_bit_cast(float, w.w & 0xffff0000u)}; } } }
; template <class Epi, class Sched, bool ALIGN_EPI = false, bool SP2 = false, bool F8 = false>
; __device__ __forceinline__ void gemm_phase(PG8_LAS unsigned char* lds, const Gemm g, const Sched& S, const Epi& E) {
;     ...
;         PG8_STAGE(PG8_SB(0, 0), cB, voffB); PG8_STAGE(PG8_SB(0, 1), cB + hstep, voffB); PG8_STAGE(PG8_SA(0, 0), cA, voffA); PG8_STAGE(PG8_SA(0, 1), cA + hstep, voffA);
;         if (wr == 1) PG8_BAR;
;         PG8_WAIT_V(2); PG8_BAR;
;         PG8_STAGE(PG8_SB(1, 0), cB + kstep, voffB); PG8_STAGE(PG8_SA(1, 0), cA + kstep, voffA); PG8_STAGE(PG8_SB(1, 1), cB + hstep + kstep, voffB);
;         PG8_WAIT_V(6); PG8_BAR;
.LBB0_1057:
	s_mov_b64 s[22:23], 0x80
	s_add_i32 m0, s17, 0x18000
	v_lshl_add_u64 v[116:117], v[116:117], 0, s[22:23]
	s_lshl_b32 s0, s6, 13
	s_lshl_b32 s1, s5, 12
	s_waitcnt vmcnt(2)
	s_barrier
	global_load_lds_dwordx4 v[116:117], off
	v_lshl_add_u64 v[114:115], v[114:115], 0, s[22:23]
	s_add_i32 m0, s17, 0x1a000
	s_add_i32 s70, s17, 0x8000
	s_add_i32 s71, s17, 0xa000
	global_load_lds_dwordx4 v[114:115], off
	v_lshl_add_u64 v[94:95], v[94:95], 0, s[22:23]
	s_mov_b32 m0, s70
	s_add_u32 s6, s44, 0x20080
	global_load_lds_dwordx4 v[94:95], off
	v_lshl_add_u64 v[94:95], v[96:97], 0, s[22:23]
	s_mov_b32 m0, s71
	s_addc_u32 s7, s45, 0
	global_load_lds_dwordx4 v[94:95], off
	s_add_i32 m0, s17, 0x1c000
	v_lshl_add_u64 v[94:95], s[6:7], 0, v[132:133]
	global_load_lds_dwordx4 v[94:95], off
	v_lshl_add_u64 v[94:95], s[6:7], 0, v[136:137]
	s_add_i32 m0, s17, 0x1e000
	s_waitcnt lgkmcnt(0)
	v_lshlrev_b32_e32 v147, 6, v1
	global_load_lds_dwordx4 v[94:95], off
	v_lshlrev_b32_e32 v140, 4, v140
	s_movk_i32 s5, 0x3c0
	v_and_or_b32 v147, v147, s5, v140
	v_lshl_or_b32 v140, v146, 6, v140
	v_lshlrev_b32_e32 v146, 2, v146
	v_and_b32_e32 v146, 32, v146
	v_bitop3_b32 v157, v140, s1, v146 bitop3:0xde
	v_lshlrev_b32_e32 v140, 13, v138
	v_and_b32_e32 v140, 0xffffc000, v140
	v_lshl_add_u32 v139, v139, 10, v140
	v_and_b32_e32 v138, 1, v138
	v_lshlrev_b32_e32 v140, 13, v142
	v_lshl_or_b32 v138, v138, 6, v139
	v_and_b32_e32 v140, 0xffffc000, v140
	v_lshlrev_b32_e32 v148, 2, v1
	v_lshl_add_u32 v138, v141, 1, v138
	v_lshl_add_u32 v140, v143, 10, v140
	v_and_b32_e32 v141, 1, v142
	v_and_b32_e32 v148, 32, v148
	s_waitcnt vmcnt(6)
	v_lshl_or_b32 v140, v141, 6, v140
	v_bitop3_b32 v147, v147, s0, v148 bitop3:0xde
	s_mov_b64 s[6:7], 0x20080
	s_cmpk_lt_u32 s3, 0x100
	v_mov_b32_e32 v139, v133
	v_lshl_add_u32 v140, v144, 1, v140
	v_mov_b32_e32 v141, v133
	s_waitcnt vmcnt(6)
	v_lshlrev_b32_e32 v54, 16, v14
	v_and_b32_e32 v55, 0xffff0000, v14
	v_lshlrev_b32_e32 v56, 16, v15
	v_and_b32_e32 v57, 0xffff0000, v15
	v_lshlrev_b32_e32 v50, 16, v16
	v_and_b32_e32 v51, 0xffff0000, v16
	v_lshlrev_b32_e32 v52, 16, v17
	v_and_b32_e32 v53, 0xffff0000, v17
	v_lshlrev_b32_e32 v14, 16, v10
	v_and_b32_e32 v15, 0xffff0000, v10
	v_lshlrev_b32_e32 v16, 16, v11
	v_and_b32_e32 v17, 0xffff0000, v11
	v_lshlrev_b32_e32 v10, 16, v12
	v_and_b32_e32 v11, 0xffff0000, v12
	v_lshlrev_b32_e32 v12, 16, v13
	v_and_b32_e32 v13, 0xffff0000, v13
	v_lshlrev_b32_e32 v70, 16, v22
	v_and_b32_e32 v71, 0xffff0000, v22
	v_lshlrev_b32_e32 v72, 16, v23
	v_and_b32_e32 v73, 0xffff0000, v23
	v_lshlrev_b32_e32 v66, 16, v24
	v_and_b32_e32 v67, 0xffff0000, v24
	v_lshlrev_b32_e32 v68, 16, v25
	v_and_b32_e32 v69, 0xffff0000, v25
	v_lshlrev_b32_e32 v22, 16, v18
	v_and_b32_e32 v23, 0xffff0000, v18
	v_lshlrev_b32_e32 v24, 16, v19
	v_and_b32_e32 v25, 0xffff0000, v19
	v_lshlrev_b32_e32 v18, 16, v20
	v_and_b32_e32 v19, 0xffff0000, v20
	v_lshlrev_b32_e32 v20, 16, v21
	v_and_b32_e32 v21, 0xffff0000, v21
	v_lshlrev_b32_e32 v78, 16, v30
	v_and_b32_e32 v79, 0xffff0000, v30
	v_lshlrev_b32_e32 v80, 16, v31
	v_and_b32_e32 v81, 0xffff0000, v31
	v_lshlrev_b32_e32 v74, 16, v32
	v_and_b32_e32 v75, 0xffff0000, v32
	v_lshlrev_b32_e32 v76, 16, v33
	v_and_b32_e32 v77, 0xffff0000, v33
	v_lshlrev_b32_e32 v30, 16, v26
	v_and_b32_e32 v31, 0xffff0000, v26
	v_lshlrev_b32_e32 v32, 16, v27
	v_and_b32_e32 v33, 0xffff0000, v27
	v_lshlrev_b32_e32 v26, 16, v28
	v_and_b32_e32 v27, 0xffff0000, v28
	v_lshlrev_b32_e32 v28, 16, v29
	v_and_b32_e32 v29, 0xffff0000, v29
	v_lshlrev_b32_e32 v86, 16, v38
	v_and_b32_e32 v87, 0xffff0000, v38
	v_lshlrev_b32_e32 v88, 16, v39
	v_and_b32_e32 v89, 0xffff0000, v39
	v_lshlrev_b32_e32 v82, 16, v40
	v_and_b32_e32 v83, 0xffff0000, v40
	v_lshlrev_b32_e32 v84, 16, v41
	v_and_b32_e32 v85, 0xffff0000, v41
	v_lshlrev_b32_e32 v46, 16, v6
	v_and_b32_e32 v47, 0xffff0000, v6
	v_lshlrev_b32_e32 v48, 16, v7
	v_and_b32_e32 v49, 0xffff0000, v7
	v_lshlrev_b32_e32 v42, 16, v8
	v_and_b32_e32 v43, 0xffff0000, v8
	v_lshlrev_b32_e32 v44, 16, v9
	v_and_b32_e32 v45, 0xffff0000, v9
	v_lshlrev_b32_e32 v38, 16, v34
	v_and_b32_e32 v39, 0xffff0000, v34
	v_lshlrev_b32_e32 v40, 16, v35
	v_and_b32_e32 v41, 0xffff0000, v35
	v_lshlrev_b32_e32 v34, 16, v36
	v_and_b32_e32 v35, 0xffff0000, v36
	v_lshlrev_b32_e32 v36, 16, v37
	v_and_b32_e32 v37, 0xffff0000, v37
	v_lshlrev_b32_e32 v6, 16, v2
	v_and_b32_e32 v7, 0xffff0000, v2
	v_lshlrev_b32_e32 v8, 16, v3
	v_and_b32_e32 v9, 0xffff0000, v3
	v_lshlrev_b32_e32 v2, 16, v4
	v_and_b32_e32 v3, 0xffff0000, v4
	v_lshlrev_b32_e32 v4, 16, v5
	v_and_b32_e32 v5, 0xffff0000, v5
	v_lshlrev_b32_e32 v62, 16, v58
	v_and_b32_e32 v63, 0xffff0000, v58
	v_lshlrev_b32_e32 v64, 16, v59
	v_and_b32_e32 v65, 0xffff0000, v59
	v_lshlrev_b32_e32 v58, 16, v60
	v_and_b32_e32 v59, 0xffff0000, v60
	v_lshlrev_b32_e32 v60, 16, v61
	v_and_b32_e32 v61, 0xffff0000, v61
	v_lshlrev_b32_e32 v94, 16, v90
	v_and_b32_e32 v95, 0xffff0000, v90
	v_lshlrev_b32_e32 v96, 16, v91
	v_and_b32_e32 v97, 0xffff0000, v91
	v_lshlrev_b32_e32 v90, 16, v92
	v_and_b32_e32 v91, 0xffff0000, v92
	v_lshlrev_b32_e32 v92, 16, v93
	v_and_b32_e32 v93, 0xffff0000, v93
	v_lshlrev_b32_e32 v118, 16, v102
	v_and_b32_e32 v119, 0xffff0000, v102
	v_lshlrev_b32_e32 v120, 16, v103
	v_and_b32_e32 v121, 0xffff0000, v103
	v_lshlrev_b32_e32 v114, 16, v104
	v_and_b32_e32 v115, 0xffff0000, v104
	v_lshlrev_b32_e32 v116, 16, v105
	v_and_b32_e32 v117, 0xffff0000, v105
	v_lshlrev_b32_e32 v102, 16, v98
	v_and_b32_e32 v103, 0xffff0000, v98
	v_lshlrev_b32_e32 v104, 16, v99
	v_and_b32_e32 v105, 0xffff0000, v99
	v_lshlrev_b32_e32 v98, 16, v100
	v_and_b32_e32 v99, 0xffff0000, v100
	v_lshlrev_b32_e32 v100, 16, v101
	v_and_b32_e32 v101, 0xffff0000, v101
	v_lshlrev_b32_e32 v126, 16, v110
	v_and_b32_e32 v127, 0xffff0000, v110
	v_lshlrev_b32_e32 v128, 16, v111
	v_and_b32_e32 v129, 0xffff0000, v111
	v_lshlrev_b32_e32 v122, 16, v112
	v_and_b32_e32 v123, 0xffff0000, v112
	v_lshlrev_b32_e32 v124, 16, v113
	v_and_b32_e32 v125, 0xffff0000, v113
	v_lshlrev_b32_e32 v110, 16, v106
	v_and_b32_e32 v111, 0xffff0000, v106
	v_lshlrev_b32_e32 v112, 16, v107
	v_and_b32_e32 v113, 0xffff0000, v107
	v_lshlrev_b32_e32 v106, 16, v108
	v_and_b32_e32 v107, 0xffff0000, v108
	v_lshlrev_b32_e32 v108, 16, v109
	v_and_b32_e32 v109, 0xffff0000, v109
	s_cselect_b64 s[24:25], -1, 0
	v_or_b32_e32 v158, s4, v145
	v_lshl_add_u64 v[138:139], v[138:139], 0, s[6:7]
	v_lshl_add_u64 v[140:141], v[140:141], 0, s[6:7]
	v_mov_b64_e32 v[142:143], 0x100
	v_mov_b64_e32 v[144:145], 0xff
	s_add_i32 s72, 0, 0x10000
	s_add_i32 s73, 0, 0x14000
	v_add_u32_e32 v159, 0, v147
	s_barrier
	s_branch .LBB0_1059
